# v27 + static priority for waves 4-7 through the attention phase (set before the unit loop, reset after)
# speedup vs baseline: 1.0030x; 1.0005x over previous
.LBB0_650:
	s_lshl_b32 s2, s2, 3
	s_ashr_i32 s3, s2, 31
	v_readlane_b32 s12, v253, 20
	s_xor_b32 s3, s3, s12
	s_abs_i32 s2, s2
	v_readlane_b32 s12, v254, 33
	s_mul_hi_u32 s12, s2, s12
	v_readlane_b32 s17, v254, 32
	s_mul_i32 s13, s12, s17
	s_sub_i32 s2, s2, s13
	s_add_i32 s13, s12, 1
	s_sub_i32 s16, s2, s17
	s_cmp_ge_u32 s2, s17
	s_cselect_b32 s12, s13, s12
	s_cselect_b32 s2, s16, s2
	s_add_i32 s13, s12, 1
	s_cmp_ge_u32 s2, s17
	s_cselect_b32 s2, s13, s12
	s_xor_b32 s2, s2, s3
	s_sub_i32 s2, s2, s3
	s_and_b32 s12, s2, 7
	v_readlane_b32 s2, v253, 32
	v_readlane_b32 s3, v253, 33
	s_lshl_b32 s2, s2, 8
	s_lshl_b32 s3, s12, 5
	s_or_b32 s96, s3, s2
	s_lshl_b64 s[2:3], s[96:97], 2
	v_readlane_b32 s13, v254, 22
	s_add_u32 s52, s13, s2
	v_readlane_b32 s2, v254, 23
	s_addc_u32 s53, s2, s3
	s_mul_i32 s2, s12, 0x2800000
	s_add_u32 s78, s24, s2
	s_addc_u32 s79, s25, 0
	s_add_u32 s28, s78, 0x4d000000
	s_addc_u32 s29, s79, 0
	s_add_u32 s54, s78, 0x4d000400
	s_addc_u32 s55, s79, 0
	s_add_u32 s56, s78, 0x4d000800
	s_addc_u32 s57, s79, 0
	s_add_u32 s2, s14, s2
	s_addc_u32 s3, s15, 0
	s_add_u32 s58, s2, 0x91000000
	s_addc_u32 s59, s3, 0
	s_lshl_b32 s2, s12, 17
	s_add_u32 s0, s0, s2
	s_addc_u32 s1, s1, 0
	s_add_u32 s60, s0, 0x6d900000
	s_addc_u32 s61, s1, 0
	v_readfirstlane_b32 s2, v0
	s_cmp_lt_u32 s2, 0x100
	s_cbranch_scc1 .Lattn_prio0
	s_setprio 1
.Lattn_prio0:
	s_branch .LBB0_653
.LBB0_651:
	s_or_b64 exec, exec, s[0:1]
	s_waitcnt lgkmcnt(0)
	ds_read_b128 v[34:37], v192 offset:53376
	ds_read_b128 v[38:41], v192 offset:53408
	s_add_u32 s0, s58, s42
	s_addc_u32 s1, s59, s43
	s_lshl_b32 s2, s3, 12
	s_waitcnt lgkmcnt(1)
	v_rcp_f32_e32 v42, v34
	v_rcp_f32_e32 v43, v35
	s_add_i32 s2, s2, 0
	v_lshlrev_b32_e32 v50, 1, v184
	v_lshlrev_b32_e32 v51, 9, v183
	v_mul_f32_e32 v2, v2, v42
	v_add3_u32 v50, s2, v50, v51
	v_cvt_pk_bf16_f32 v2, v2, s0
	v_rcp_f32_e32 v44, v36
	v_rcp_f32_e32 v45, v37
	s_waitcnt lgkmcnt(0)
	v_rcp_f32_e32 v46, v38
	ds_read_b128 v[34:37], v192 offset:53440
	v_rcp_f32_e32 v47, v39
	v_rcp_f32_e32 v48, v40
	v_rcp_f32_e32 v49, v41
	ds_read_b128 v[38:41], v192 offset:53472
	ds_write_b16 v50, v2 offset:55360
	v_mul_f32_e32 v2, v19, v43
	v_cvt_pk_bf16_f32 v2, v2, s0
	ds_write_b16 v50, v2 offset:55424
	v_mul_f32_e32 v2, v3, v43
	v_cvt_pk_bf16_f32 v2, v2, s0
	ds_write_b16 v50, v2 offset:55488
	v_mul_f32_e32 v2, v20, v44
	v_cvt_pk_bf16_f32 v2, v2, s0
	ds_write_b16 v50, v2 offset:55552
	v_mul_f32_e32 v2, v4, v44
	v_cvt_pk_bf16_f32 v2, v2, s0
	ds_write_b16 v50, v2 offset:55616
	v_mul_f32_e32 v2, v21, v45
	v_cvt_pk_bf16_f32 v2, v2, s0
	ds_write_b16 v50, v2 offset:55680
	v_mul_f32_e32 v2, v5, v45
	v_cvt_pk_bf16_f32 v2, v2, s0
	ds_write_b16 v50, v2 offset:55744
	v_mul_f32_e32 v2, v22, v46
	v_cvt_pk_bf16_f32 v2, v2, s0
	ds_write_b16 v50, v2 offset:56320
	v_mul_f32_e32 v2, v6, v46
	v_cvt_pk_bf16_f32 v2, v2, s0
	ds_write_b16 v50, v2 offset:56384
	v_mul_f32_e32 v2, v23, v47
	v_cvt_pk_bf16_f32 v2, v2, s0
	ds_write_b16 v50, v2 offset:56448
	v_mul_f32_e32 v2, v7, v47
	v_cvt_pk_bf16_f32 v2, v2, s0
	ds_write_b16 v50, v2 offset:56512
	v_mul_f32_e32 v2, v24, v48
	v_cvt_pk_bf16_f32 v2, v2, s0
	ds_write_b16 v50, v2 offset:56576
	v_mul_f32_e32 v2, v8, v48
	v_cvt_pk_bf16_f32 v2, v2, s0
	s_waitcnt lgkmcnt(13)
	v_rcp_f32_e32 v34, v34
	ds_write_b16 v50, v2 offset:56640
	v_mul_f32_e32 v2, v25, v49
	v_cvt_pk_bf16_f32 v2, v2, s0
	ds_write_b16 v50, v2 offset:56704
	v_mul_f32_e32 v2, v9, v49
	v_cvt_pk_bf16_f32 v2, v2, s0
	v_rcp_f32_e32 v35, v35
	ds_write_b16 v50, v2 offset:56768
	v_mul_f32_e32 v2, v26, v34
	v_cvt_pk_bf16_f32 v2, v2, s0
	ds_write_b16 v50, v2 offset:57344
	v_mul_f32_e32 v2, v10, v34
	v_cvt_pk_bf16_f32 v2, v2, s0
	v_rcp_f32_e32 v36, v36
	ds_write_b16 v50, v2 offset:57408
	v_mul_f32_e32 v2, v27, v35
	v_cvt_pk_bf16_f32 v2, v2, s0
	ds_write_b16 v50, v2 offset:57472
	v_mul_f32_e32 v2, v11, v35
	v_cvt_pk_bf16_f32 v2, v2, s0
	v_rcp_f32_e32 v37, v37
	ds_write_b16 v50, v2 offset:57536
	v_mul_f32_e32 v2, v28, v36
	v_cvt_pk_bf16_f32 v2, v2, s0
	ds_write_b16 v50, v2 offset:57600
	v_mul_f32_e32 v2, v12, v36
	v_cvt_pk_bf16_f32 v2, v2, s0
	s_waitcnt lgkmcnt(14)
	v_rcp_f32_e32 v38, v38
	ds_write_b16 v50, v2 offset:57664
	v_mul_f32_e32 v2, v29, v37
	v_cvt_pk_bf16_f32 v2, v2, s0
	ds_write_b16 v50, v2 offset:57728
	v_mul_f32_e32 v2, v13, v37
	v_cvt_pk_bf16_f32 v2, v2, s0
	v_rcp_f32_e32 v39, v39
	ds_write_b16 v50, v2 offset:57792
	v_mul_f32_e32 v2, v30, v38
	v_cvt_pk_bf16_f32 v2, v2, s0
	ds_write_b16 v50, v2 offset:58368
	v_mul_f32_e32 v2, v14, v38
	v_cvt_pk_bf16_f32 v2, v2, s0
	v_rcp_f32_e32 v40, v40
	ds_write_b16 v50, v2 offset:58432
	v_mul_f32_e32 v2, v31, v39
	v_cvt_pk_bf16_f32 v2, v2, s0
	ds_write_b16 v50, v2 offset:58496
	v_mul_f32_e32 v2, v15, v39
	v_cvt_pk_bf16_f32 v2, v2, s0
	v_rcp_f32_e32 v41, v41
	ds_write_b16 v50, v2 offset:58560
	v_mul_f32_e32 v2, v32, v40
	v_cvt_pk_bf16_f32 v2, v2, s0
	ds_write_b16 v50, v2 offset:58624
	v_mul_f32_e32 v2, v16, v40
	v_cvt_pk_bf16_f32 v2, v2, s0
	ds_write_b16 v50, v2 offset:58688
	v_mul_f32_e32 v2, v33, v41
	v_cvt_pk_bf16_f32 v2, v2, s0
	ds_write_b16 v50, v2 offset:58752
	v_mul_f32_e32 v2, v17, v41
	v_mul_f32_e32 v18, v18, v42
	v_cvt_pk_bf16_f32 v2, v2, s0
	v_cvt_pk_bf16_f32 v18, v18, s0
	ds_write_b16 v50, v2 offset:58816
	v_lshrrev_b32_e32 v1, 3, v1
	v_lshlrev_b32_e32 v2, 1, v182
	ds_write_b16 v50, v18 offset:55296
	v_and_b32_e32 v186, 0x70, v2
	v_lshlrev_b32_e32 v2, 7, v1
	s_waitcnt lgkmcnt(0)
	v_add3_u32 v10, s2, v186, v2
	s_lshl_b32 s3, s25, 1
	ds_read_b128 v[2:5], v10 offset:55296
	s_add_u32 s0, s0, s3
	s_addc_u32 s1, s1, 0
	v_mul_u32_u24_e32 v1, 0x1400, v1
	v_lshl_add_u64 v[6:7], s[0:1], 0, v[186:187]
	v_lshlrev_b32_e32 v186, 1, v1
	v_lshl_add_u64 v[6:7], v[6:7], 0, v[186:187]
	s_waitcnt lgkmcnt(0)
	global_store_dwordx4 v[6:7], v[2:5], off
	ds_read_b128 v[2:5], v10 offset:56320
	s_mov_b32 s0, 0x14000
	v_add_co_u32_e32 v8, vcc, s0, v6
	s_mov_b64 s[0:1], 0
	s_nop 0
	v_addc_co_u32_e32 v9, vcc, 0, v7, vcc
	s_waitcnt lgkmcnt(0)
	global_store_dwordx4 v[8:9], v[2:5], off
	ds_read_b128 v[2:5], v10 offset:57344
	v_add_co_u32_e32 v8, vcc, 0x28000, v6
	s_nop 1
	v_addc_co_u32_e32 v9, vcc, 0, v7, vcc
	s_waitcnt lgkmcnt(0)
	global_store_dwordx4 v[8:9], v[2:5], off
	ds_read_b128 v[2:5], v10 offset:58368
	v_add_co_u32_e32 v6, vcc, 0x3c000, v6
	s_nop 1
	v_addc_co_u32_e32 v7, vcc, 0, v7, vcc
	s_waitcnt lgkmcnt(0)
	global_store_dwordx4 v[6:7], v[2:5], off
	s_waitcnt lgkmcnt(0)
	s_barrier

.LBB0_770:
	s_setprio 0
	v_readlane_b32 s40, v253, 6
	v_readlane_b32 s14, v253, 0
	v_readlane_b32 s42, v253, 8
	v_readlane_b32 s43, v253, 9
	v_readlane_b32 s15, v253, 1
	s_mov_b64 s[0:1], s[42:43]
	s_mov_b64 s[2:3], s[14:15]
	s_waitcnt vmcnt(0) lgkmcnt(0)
	s_barrier
	s_load_dwordx2 s[2:3], s[2:3], 0x18
	v_readlane_b32 s16, v253, 32
	v_readlane_b32 s17, v253, 33
	s_add_u32 s0, s0, 0x4d000000
	s_mov_b32 s17, s97
	s_addc_u32 s1, s1, 0
	s_lshl_b64 s[12:13], s[16:17], 16
	s_waitcnt lgkmcnt(0)
	s_add_u32 s12, s2, s12
	s_addc_u32 s13, s3, s13
	s_mov_b64 s[2:3], s[14:15]
	s_load_dwordx2 s[2:3], s[2:3], 0x20
	s_mov_b32 s14, s16
	v_readlane_b32 s41, v253, 7
	v_readlane_b32 s44, v253, 10
	v_readlane_b32 s45, v253, 11
	v_readlane_b32 s46, v253, 12
	v_readlane_b32 s47, v253, 13
	v_writelane_b32 v253, s14, 32
	s_mov_b64 s[48:49], s[42:43]
	v_mov_b32_e32 v6, v0
	v_writelane_b32 v253, s15, 33
	s_lshl_b64 s[14:15], s[16:17], 10
	s_waitcnt lgkmcnt(0)
	s_add_u32 s38, s2, s14
	s_mov_b32 s2, s84
	s_addc_u32 s39, s3, s15
	v_ashrrev_i32_e32 v1, 7, v6
	v_bfe_u32 v8, v6, 5, 1
	v_and_b32_e32 v7, 31, v6
	v_lshlrev_b32_e32 v2, 12, v1
	v_lshlrev_b32_e32 v3, 9, v8
	v_or3_b32 v2, v3, v2, v7
	v_ashrrev_i32_e32 v3, 31, v2
	v_lshl_add_u64 v[2:3], v[2:3], 2, s[12:13]
	global_load_dword v98, v[2:3], off
	global_load_dword v99, v[2:3], off offset:256
	s_movk_i32 s3, 0x1000
	v_ashrrev_i32_e32 v97, 5, v6
	s_movk_i32 s13, 0x9e0
	v_mov_b32_e32 v66, 0
	v_mov_b32_e32 v70, 0
	v_mov_b32_e32 v71, 0
	v_mov_b32_e32 v72, 0
	v_mov_b32_e32 v73, 0
	global_load_dword v100, v[2:3], off offset:512
	global_load_dword v101, v[2:3], off offset:768
	global_load_dword v102, v[2:3], off offset:1024
	global_load_dword v103, v[2:3], off offset:1280
	global_load_dword v104, v[2:3], off offset:1536
	global_load_dword v105, v[2:3], off offset:1792
	global_load_dword v106, v[2:3], off offset:128
	global_load_dword v107, v[2:3], off offset:384
	global_load_dword v108, v[2:3], off offset:640
	global_load_dword v109, v[2:3], off offset:896
	global_load_dword v110, v[2:3], off offset:1152
	global_load_dword v111, v[2:3], off offset:1408
	global_load_dword v112, v[2:3], off offset:1664
	global_load_dword v113, v[2:3], off offset:1920
	v_add_co_u32_e32 v4, vcc, s3, v2
	s_movk_i32 s3, 0x2000
	s_nop 0
	v_addc_co_u32_e32 v5, vcc, 0, v3, vcc
	v_add_co_u32_e32 v10, vcc, s3, v2
	s_movk_i32 s3, 0x3000
	s_nop 0
	v_addc_co_u32_e32 v11, vcc, 0, v3, vcc
	global_load_dword v114, v[10:11], off offset:-4096
	global_load_dword v115, v[4:5], off offset:256
	v_add_co_u32_e32 v2, vcc, s3, v2
	s_lshl_b32 s3, s2, 6
	s_nop 0
	v_addc_co_u32_e32 v3, vcc, 0, v3, vcc
	s_add_i32 s12, s3, -15
	s_cmpk_lt_i32 s2, 0x200
	s_cselect_b64 s[14:15], -1, 0
	global_load_dword v116, v[4:5], off offset:512
	global_load_dword v117, v[4:5], off offset:768
	global_load_dword v118, v[4:5], off offset:1024
	global_load_dword v119, v[4:5], off offset:1280
	global_load_dword v120, v[4:5], off offset:1536
	global_load_dword v121, v[4:5], off offset:1792
	global_load_dword v122, v[4:5], off offset:128
	global_load_dword v123, v[4:5], off offset:384
	global_load_dword v124, v[4:5], off offset:640
	global_load_dword v125, v[4:5], off offset:896
	global_load_dword v126, v[4:5], off offset:1152
	global_load_dword v127, v[4:5], off offset:1408
	global_load_dword v128, v[4:5], off offset:1664
	s_nop 0
	global_load_dword v129, v[4:5], off offset:1920
	global_load_dword v130, v[10:11], off
	global_load_dword v131, v[10:11], off offset:256
	v_lshlrev_b32_e32 v9, 3, v6
	global_load_dword v132, v[10:11], off offset:512
	global_load_dword v133, v[10:11], off offset:768
	global_load_dword v134, v[10:11], off offset:1024
	global_load_dword v135, v[10:11], off offset:1280
	global_load_dword v138, v[10:11], off offset:1536
	global_load_dword v139, v[10:11], off offset:1792
	global_load_dword v140, v[10:11], off offset:128
	global_load_dword v141, v[10:11], off offset:384
	global_load_dword v142, v[10:11], off offset:640
	global_load_dword v143, v[10:11], off offset:896
	global_load_dword v144, v[10:11], off offset:1152
	global_load_dword v145, v[10:11], off offset:1408
	global_load_dword v146, v[10:11], off offset:1664
	global_load_dword v147, v[10:11], off offset:1920
	global_load_dword v148, v[2:3], off
	global_load_dword v149, v[2:3], off offset:256
	global_load_dword v150, v[2:3], off offset:512
	global_load_dword v151, v[2:3], off offset:768
	global_load_dword v152, v[2:3], off offset:1024
	global_load_dword v153, v[2:3], off offset:1280
	global_load_dword v154, v[2:3], off offset:1536
	global_load_dword v155, v[2:3], off offset:1792
	global_load_dword v156, v[2:3], off offset:128
	global_load_dword v157, v[2:3], off offset:384
	global_load_dword v158, v[2:3], off offset:640
	global_load_dword v159, v[2:3], off offset:896
	global_load_dword v160, v[2:3], off offset:1152
	global_load_dword v161, v[2:3], off offset:1408
	global_load_dword v162, v[2:3], off offset:1664
	s_nop 0
	global_load_dword v163, v[2:3], off offset:1920
	v_add_u32_e32 v3, s12, v97
	v_cmp_lt_i32_e32 vcc, -1, v3
	s_waitcnt vmcnt(0)
	v_cvt_pk_bf16_f32 v34, v98, v99
	v_cvt_pk_bf16_f32 v35, v100, v101
	v_cvt_pk_bf16_f32 v36, v102, v103
	v_cvt_pk_bf16_f32 v37, v104, v105
	v_cvt_pk_bf16_f32 v38, v106, v107
	v_cvt_pk_bf16_f32 v39, v108, v109
	v_cvt_pk_bf16_f32 v40, v110, v111
	v_cvt_pk_bf16_f32 v41, v112, v113
	v_cvt_pk_bf16_f32 v42, v114, v115
	v_cvt_pk_bf16_f32 v43, v116, v117
	v_cvt_pk_bf16_f32 v44, v118, v119
	v_cvt_pk_bf16_f32 v45, v120, v121
	v_cvt_pk_bf16_f32 v46, v122, v123
	v_cvt_pk_bf16_f32 v47, v124, v125
	v_cvt_pk_bf16_f32 v48, v126, v127
	v_cvt_pk_bf16_f32 v49, v128, v129
	v_cvt_pk_bf16_f32 v50, v130, v131
	v_cvt_pk_bf16_f32 v51, v132, v133
	v_cvt_pk_bf16_f32 v52, v134, v135
	v_cvt_pk_bf16_f32 v53, v138, v139
	v_cvt_pk_bf16_f32 v54, v140, v141
	v_cvt_pk_bf16_f32 v55, v142, v143
	v_cvt_pk_bf16_f32 v56, v144, v145
	v_cvt_pk_bf16_f32 v57, v146, v147
	v_cvt_pk_bf16_f32 v58, v148, v149
	v_cvt_pk_bf16_f32 v59, v150, v151
	v_cvt_pk_bf16_f32 v60, v152, v153
	v_cvt_pk_bf16_f32 v61, v154, v155
	v_cvt_pk_bf16_f32 v62, v156, v157
	v_cvt_pk_bf16_f32 v63, v158, v159
	v_cvt_pk_bf16_f32 v64, v160, v161
	v_cvt_pk_bf16_f32 v65, v162, v163
	v_lshlrev_b32_e32 v2, 6, v1
	v_or_b32_e32 v4, v2, v7
	v_ashrrev_i32_e32 v5, 31, v4
	v_lshl_add_u64 v[4:5], v[4:5], 2, s[38:39]
	global_load_dword v1, v[4:5], off
	global_load_dword v96, v[4:5], off offset:128
	v_cmp_gt_i32_e64 s[38:39], s13, v6
	v_and_b32_e32 v4, 0xf8, v9
	s_and_b64 s[16:17], s[14:15], s[38:39]
	s_and_b64 s[16:17], s[16:17], vcc
	v_lshlrev_b32_e32 v4, 1, v4
	s_and_saveexec_b64 s[24:25], s[16:17]
	s_cbranch_execz .LBB0_772
	v_mov_b64_e32 v[10:11], s[0:1]
	s_movk_i32 s13, 0x2800
	v_mad_u64_u32 v[10:11], s[16:17], v3, s13, v[10:11]
	v_mov_b32_e32 v5, v187
	v_lshl_add_u64 v[10:11], v[10:11], 0, v[4:5]
	global_load_dwordx4 v[70:73], v[10:11], off offset:3072
